# add HGRN2 state-update operand reads hoisted with counted lgkmcnt (opt9)
# speedup vs baseline: 1.0048x; 1.0002x over previous
; #define LAS __attribute__((address_space(3)))
; __device__ __forceinline__ v2u pack4(f32x4 v) { v2u w; w.x = pk2(v[0], v[1]); w.y = pk2(v[2], v[3]); return w; }
; __device__ __forceinline__ void hgrn_chunk_scan(Frame& F, const Args& args, int bh) {
;     ...
;         if (wave < 4) { const int tt = wave >> 1, st = wave & 1;
;             f32x4 a = mm16<4>(KD + 16 * st * PQ, PQ, QD + 16 * tt * PQ, PQ, (f32x4){0.f, 0.f, 0.f, 0.f}, lane);
;             const int t = 16 * tt + r16, s0 = 16 * st + 4 * q4;
; #pragma unroll
;             for (int i = 0; i < 4; ++i) a[i] = (s0 + i <= t) ? a[i] : 0.f;
;             *(LAS v2u*)(AT + t * PS + s0) = pack4(a); }
;         const int ott = wave & 1, ovt0 = 2 * (wave >> 1);
;         f32x4 o0 = mm16<4>(QD + 16 * ott * PQ, PQ, ST + 16 * ovt0 * PQ, PQ, (f32x4){0.f, 0.f, 0.f, 0.f}, lane);
;         f32x4 o1 = mm16<4>(QD + 16 * ott * PQ, PQ, ST + 16 * (ovt0 + 1) * PQ, PQ, (f32x4){0.f, 0.f, 0.f, 0.f}, lane);
;         __syncthreads();
;         o0 = mm16<1>(AT + 16 * ott * PS, PS, VT + 16 * ovt0 * PS, PS, o0, lane);
;         o1 = mm16<1>(AT + 16 * ott * PS, PS, VT + 16 * (ovt0 + 1) * PS, PS, o1, lane);
; #pragma unroll
;         for (int i = 0; i < 4; ++i) { OB[(16 * ott + 4 * q4 + i) * PO + 16 * ovt0 + r16] = o0[i]; OB[(16 * ott + 4 * q4 + i) * PO + 16 * (ovt0 + 1) + r16] = o1[i]; }
;         {
;             const f32x4 de = *(const LAS f32x4*)(DEND + 16 * wave + 4 * q4);
; #pragma unroll
;             for (int vt = 0; vt < 8; ++vt) { Sacc[vt] = Sacc[vt] * de; Sacc[vt] = mm16<1>(KET + 16 * wave * PS, PS, VT + 16 * vt * PS, PS, Sacc[vt], lane);
;                 *(LAS v2u*)(ST + (16 * vt + r16) * PQ + 16 * wave + 4 * q4) = pack4(Sacc[vt]); }
;         }
.LBB0_829:
	v_lshlrev_b32_e32 v97, 1, v56
	v_add3_u32 v110, s66, v50, v97
	v_add3_u32 v111, s18, v50, v97
	ds_read_b128 v[54:57], v110
	ds_read_b128 v[68:71], v111 offset:37888
	ds_read_b128 v[98:101], v110 offset:64
	ds_read_b128 v[102:105], v111 offset:37952
	v_add3_u32 v114, s68, v50, v97
	v_mul_lo_u32 v52, v52, s33
	s_waitcnt lgkmcnt(2)
	v_mfma_f32_16x16x32_bf16 v[68:71], v[54:57], v[68:71], 0
	v_add_u32_e32 v52, s58, v52
	s_lshl_b32 s0, s19, 2
	s_waitcnt lgkmcnt(0)
	v_mfma_f32_16x16x32_bf16 v[68:71], v[98:101], v[102:105], v[68:71]
	ds_read_b128 v[102:105], v110 offset:128
	ds_read_b128 v[106:109], v111 offset:38016
	s_waitcnt lgkmcnt(0)
	v_mfma_f32_16x16x32_bf16 v[68:71], v[102:105], v[106:109], v[68:71]
	ds_read_b128 v[106:109], v110 offset:192
	ds_read_b128 v[110:113], v111 offset:38080
	s_waitcnt lgkmcnt(0)
	v_mfma_f32_16x16x32_bf16 v[68:71], v[106:109], v[110:113], v[68:71]
	ds_read_b128 v[110:113], v114 offset:37888
	s_waitcnt lgkmcnt(0)
	v_mfma_f32_16x16x32_bf16 v[54:57], v[54:57], v[110:113], 0
	ds_read_b128 v[110:113], v114 offset:37952
	s_waitcnt lgkmcnt(0)
	v_mfma_f32_16x16x32_bf16 v[54:57], v[98:101], v[110:113], v[54:57]
	ds_read_b128 v[98:101], v114 offset:38016
	s_waitcnt lgkmcnt(0)
	v_mfma_f32_16x16x32_bf16 v[54:57], v[102:105], v[98:101], v[54:57]
	ds_read_b128 v[98:101], v114 offset:38080
	s_waitcnt lgkmcnt(0)
	s_barrier
	v_mfma_f32_16x16x32_bf16 v[54:57], v[106:109], v[98:101], v[54:57]
	v_mul_u32_u24_e32 v98, 40, v51
	v_lshlrev_b32_e32 v106, 1, v98
	v_mul_u32_u24_e32 v107, 0x50, v51
	v_add3_u32 v98, s69, v106, v97
	v_add3_u32 v102, s70, v107, v97
	ds_read_b128 v[98:101], v98
	ds_read_b128 v[102:105], v102 offset:17408
	s_waitcnt lgkmcnt(0)
	v_mfma_f32_16x16x32_bf16 v[68:71], v[98:101], v[102:105], v[68:71]
	v_add3_u32 v102, s71, v107, v97
	ds_read_b128 v[102:105], v102 offset:17408
	v_lshlrev_b32_e32 v51, 2, v51
	s_waitcnt lgkmcnt(0)
	v_mfma_f32_16x16x32_bf16 v[54:57], v[98:101], v[102:105], v[54:57]
	v_add3_u32 v98, v52, s67, v51
	v_add3_u32 v51, v52, s0, v51
	s_nop 0
	ds_write_b32 v98, v68
	s_nop 3
	ds_write_b32 v51, v54
	ds_write_b32 v98, v69 offset:528
	ds_write_b32 v51, v55 offset:528
	ds_write_b32 v98, v70 offset:1056
	ds_write_b32 v51, v56 offset:1056
	ds_write_b32 v98, v71 offset:1584
	ds_write_b32 v51, v57 offset:1584
	v_lshl_add_u32 v51, v53, 2, s60
	ds_read_b128 v[54:57], v51
	v_add3_u32 v102, s61, v106, v97
	v_add3_u32 v97, 0, v107, v97
	ds_read_b128 v[68:71], v102 offset:27648
	ds_read_b128 v[244:247], v97 offset:17408
	ds_read_b128 v[212:215], v97 offset:18688
	ds_read_b128 v[216:219], v97 offset:19968
	ds_read_b128 v[220:223], v97 offset:21248
	ds_read_b128 v[228:231], v97 offset:22528
	ds_read_b128 v[232:235], v97 offset:23808
	ds_read_b128 v[236:239], v97 offset:25088
	ds_read_b128 v[240:243], v97 offset:26368
	v_lshlrev_b32_e32 v51, 1, v53
	v_add3_u32 v98, s78, v51, v50
	v_add_u32_e32 v99, 0x9400, v98
	s_waitcnt lgkmcnt(9)
	v_pk_mul_f32 v[44:45], v[44:45], v[56:57]
	v_pk_mul_f32 v[42:43], v[42:43], v[54:55]
	v_pk_mul_f32 v[40:41], v[40:41], v[56:57]
	v_pk_mul_f32 v[38:39], v[38:39], v[54:55]
	v_pk_mul_f32 v[36:37], v[36:37], v[56:57]
	v_pk_mul_f32 v[34:35], v[34:35], v[54:55]
	v_pk_mul_f32 v[32:33], v[32:33], v[56:57]
	v_pk_mul_f32 v[30:31], v[30:31], v[54:55]
	v_mul_f32_e64 v28, v28, v56
	v_mul_f32_e64 v29, v29, v57
	v_pk_mul_f32 v[26:27], v[26:27], v[54:55]
	v_pk_mul_f32 v[24:25], v[24:25], v[56:57]
	v_mul_f32_e64 v22, v22, v54
	v_mul_f32_e64 v23, v23, v55
	v_pk_mul_f32 v[16:17], v[16:17], v[56:57]
	v_pk_mul_f32 v[14:15], v[14:15], v[54:55]
	v_mul_f32_e64 v12, v12, v56
	v_mul_f32_e64 v13, v13, v57
	v_pk_mul_f32 v[10:11], v[10:11], v[54:55]
	s_nop 1
	s_waitcnt lgkmcnt(7)
	v_mfma_f32_16x16x32_bf16 v[42:45], v[68:71], v[244:247], v[42:45]
	s_waitcnt lgkmcnt(6)
	v_mfma_f32_16x16x32_bf16 v[38:41], v[68:71], v[212:215], v[38:41]
	s_waitcnt lgkmcnt(5)
	v_mfma_f32_16x16x32_bf16 v[34:37], v[68:71], v[216:219], v[34:37]
	s_waitcnt lgkmcnt(4)
	v_mfma_f32_16x16x32_bf16 v[30:33], v[68:71], v[220:223], v[30:33]
	s_waitcnt lgkmcnt(3)
	v_mfma_f32_16x16x32_bf16 v[26:29], v[68:71], v[228:231], v[26:29]
	s_waitcnt lgkmcnt(2)
	v_mfma_f32_16x16x32_bf16 v[22:25], v[68:71], v[232:235], v[22:25]
	s_waitcnt lgkmcnt(1)
	v_mfma_f32_16x16x32_bf16 v[14:17], v[68:71], v[236:239], v[14:17]
	s_waitcnt lgkmcnt(0)
	v_mfma_f32_16x16x32_bf16 v[10:13], v[68:71], v[240:243], v[10:13]
	s_nop 1
	v_cvt_pk_bf16_f32 v50, v42, v43
	v_cvt_pk_bf16_f32 v51, v44, v45
	ds_write_b64 v98, v[50:51] offset:37888
	v_cvt_pk_bf16_f32 v52, v38, v39
	v_cvt_pk_bf16_f32 v53, v40, v41
	ds_write_b64 v98, v[52:53] offset:42240
	v_cvt_pk_bf16_f32 v50, v34, v35
	v_cvt_pk_bf16_f32 v51, v36, v37
	ds_write_b64 v98, v[50:51] offset:46592
	v_cvt_pk_bf16_f32 v52, v30, v31
	v_cvt_pk_bf16_f32 v53, v32, v33
	ds_write_b64 v98, v[52:53] offset:50944
	v_cvt_pk_bf16_f32 v50, v26, v27
	v_cvt_pk_bf16_f32 v51, v28, v29
	ds_write_b64 v98, v[50:51] offset:55296
	v_cvt_pk_bf16_f32 v52, v22, v23
	v_cvt_pk_bf16_f32 v53, v24, v25
	ds_write_b64 v98, v[52:53] offset:59648
	v_cvt_pk_bf16_f32 v50, v14, v15
	v_cvt_pk_bf16_f32 v51, v16, v17
	ds_write_b64 v98, v[50:51] offset:64000
	v_cvt_pk_bf16_f32 v52, v10, v11
	v_cvt_pk_bf16_f32 v53, v12, v13
	ds_write_b64 v99, v[52:53] offset:30464
	v_ashrrev_i32_e32 v50, 4, v58
	v_ashrrev_i32_e32 v51, 31, v50
	v_lshl_add_u64 v[68:69], s[72:73], 0, v[50:51]
	v_lshlrev_b32_e32 v51, 3, v58
	v_and_b32_e32 v70, 0x78, v51
	v_mul_lo_u32 v50, v50, s33
	v_lshlrev_b32_e32 v51, 2, v70
	v_add3_u32 v50, s58, v50, v51
	s_waitcnt lgkmcnt(0)
	s_barrier
; #define GAS __attribute__((address_space(1)))
; #define LAS __attribute__((address_space(3)))
; __device__ __forceinline__ unsigned pk2(float lo, float hi) { const f32x2 v = {lo, hi}; const bf16x2_hw r = __builtin_convertvector(v, bf16x2_hw); return __builtin_bit_cast(unsigned, r); }
; __device__ __forceinline__ float bflo(unsigned w) { return __uint_as_float(w << 16); }
; __device__ __forceinline__ float bfhi(unsigned w) { return __uint_as_float(w & 0xffff0000u); }
; __device__ __forceinline__ float sigmoidf_(float x) { return __builtin_amdgcn_rcpf(1.0f + __expf(-x)); }
; __device__ __forceinline__ void hgrn_chunk_scan(Frame& F, const Args& args, int bh) {
;     ...
;         {
;             const int t = tid >> 4, vg = tid & 15; const size_t m = (size_t)b * SEQ + ch * CL + t;
;             const f32x4 x0 = *(const LAS f32x4*)(OB + t * PO + 8 * vg), x1 = *(const LAS f32x4*)(OB + t * PO + 8 * vg + 4);
;             float ss = (x0[0] * x0[0] + x0[1] * x0[1]) + (x0[2] * x0[2] + x0[3] * x0[3]) + ((x1[0] * x1[0] + x1[1] * x1[1]) + (x1[2] * x1[2] + x1[3] * x1[3]));
;             ss = row16_sum(ss);
;             const float rs = __builtin_amdgcn_rsqf(ss * (1.0f / 128.0f) + NORM_EPS);
;             const v4u og = ogc; ogc = ogn;
;             const float z0 = bflo(og.x), z1 = bfhi(og.x), z2 = bflo(og.y), z3 = bfhi(og.y), z4 = bflo(og.z), z5 = bfhi(og.z), z6 = bflo(og.w), z7 = bfhi(og.w);
;             v4u w; w.x = pk2(x0[0] * rs * gng0 * (z0 * sigmoidf_(z0)), x0[1] * rs * gng1 * (z1 * sigmoidf_(z1))); w.y = pk2(x0[2] * rs * gng2 * (z2 * sigmoidf_(z2)), x0[3] * rs * gng3 * (z3 * sigmoidf_(z3)));
;             w.z = pk2(x1[0] * rs * gng4 * (z4 * sigmoidf_(z4)), x1[1] * rs * gng5 * (z5 * sigmoidf_(z5))); w.w = pk2(x1[2] * rs * gng6 * (z6 * sigmoidf_(z6)), x1[3] * rs * gng7 * (z7 * sigmoidf_(z7)));
;             *(GAS v4u*)(YB + m * 1024 + h * 128 + 8 * vg) = w;
;         }
	ds_read_b128 v[54:57], v50
	ds_read_b128 v[50:53], v50 offset:16
	s_add_u32 s72, s72, 32
	s_addc_u32 s73, s73, 0
	s_add_u32 s80, s80, 0xb8000
	s_waitcnt lgkmcnt(1)
	v_mov_b32_e32 v100, v55
	s_waitcnt lgkmcnt(0)
	v_mov_b32_e32 v101, v51
	v_mov_b32_e32 v98, v54
	v_mov_b32_e32 v99, v50
	v_pk_mul_f32 v[100:101], v[100:101], v[100:101]
	v_mov_b32_e32 v102, v57
	v_mov_b32_e32 v103, v53
	v_pk_fma_f32 v[98:99], v[98:99], v[98:99], v[100:101]
	v_mov_b32_e32 v100, v56
	v_mov_b32_e32 v101, v52
	v_pk_mul_f32 v[102:103], v[102:103], v[102:103]
	s_addc_u32 s81, s81, 0
	v_pk_fma_f32 v[100:101], v[100:101], v[100:101], v[102:103]
	s_cmp_lg_u32 s80, 0x2e00000
	v_pk_add_f32 v[98:99], v[98:99], v[100:101]
	s_nop 0
	v_add_f32_e32 v58, v98, v99
	v_lshlrev_b32_e32 v98, 16, v18
	v_and_b32_e32 v99, 0xffff0000, v18
	v_mul_f32_e32 v18, 0xbfb8aa3b, v98
	v_exp_f32_e32 v18, v18
	v_add_f32_dpp v58, v58, v58 quad_perm:[1,0,3,2] row_mask:0xf bank_mask:0xf bound_ctrl:1
	v_add_f32_e32 v18, 1.0, v18
	v_rcp_f32_e32 v100, v18
	v_mul_f32_e32 v18, 0xbfb8aa3b, v99
	v_add_f32_dpp v58, v58, v58 quad_perm:[2,3,0,1] row_mask:0xf bank_mask:0xf bound_ctrl:1
	v_exp_f32_e32 v18, v18
	s_nop 0
	v_add_f32_dpp v58, v58, v58 row_half_mirror row_mask:0xf bank_mask:0xf bound_ctrl:1
	v_add_f32_e32 v18, 1.0, v18
	s_nop 0
	v_add_f32_dpp v58, v58, v58 row_mirror row_mask:0xf bank_mask:0xf bound_ctrl:1
	v_fmamk_f32 v58, v58, 0x3c000000, v80
	v_rsq_f32_e32 v58, v58
	v_rcp_f32_e32 v101, v18
	v_pk_mul_f32 v[54:55], v[54:55], v[58:59] op_sel_hi:[1,0]
	s_nop 0
	v_pk_mul_f32 v[54:55], v[6:7], v[54:55]
	v_pk_mul_f32 v[98:99], v[100:101], v[98:99]
	v_pk_mul_f32 v[56:57], v[56:57], v[58:59] op_sel_hi:[1,0]
	v_pk_mul_f32 v[54:55], v[98:99], v[54:55]
	v_pk_mul_f32 v[56:57], v[8:9], v[56:57]
	v_cvt_pk_bf16_f32 v18, v54, v55
	v_lshlrev_b32_e32 v54, 16, v19
	v_and_b32_e32 v55, 0xffff0000, v19
	v_mul_f32_e32 v19, 0xbfb8aa3b, v54
	v_exp_f32_e32 v19, v19
	v_pk_mul_f32 v[50:51], v[50:51], v[58:59] op_sel_hi:[1,0]
	v_pk_mul_f32 v[52:53], v[52:53], v[58:59] op_sel_hi:[1,0]
	v_pk_mul_f32 v[50:51], v[2:3], v[50:51]
	v_add_f32_e32 v19, 1.0, v19
	v_rcp_f32_e32 v98, v19
	v_mul_f32_e32 v19, 0xbfb8aa3b, v55
	v_exp_f32_e32 v19, v19
	v_pk_mul_f32 v[52:53], v[4:5], v[52:53]
	v_lshlrev_b32_e32 v58, 1, v70
	v_add_f32_e32 v19, 1.0, v19
	v_rcp_f32_e32 v99, v19
	s_nop 0
	v_pk_mul_f32 v[54:55], v[98:99], v[54:55]
	s_nop 0
	v_pk_mul_f32 v[54:55], v[54:55], v[56:57]
	s_nop 0
	v_cvt_pk_bf16_f32 v19, v54, v55
	v_lshlrev_b32_e32 v54, 16, v20
	v_and_b32_e32 v55, 0xffff0000, v20
	v_mul_f32_e32 v20, 0xbfb8aa3b, v54
	v_exp_f32_e32 v20, v20
	s_nop 0
	v_add_f32_e32 v20, 1.0, v20
	v_rcp_f32_e32 v56, v20
	v_mul_f32_e32 v20, 0xbfb8aa3b, v55
	v_exp_f32_e32 v20, v20
	s_nop 0
	v_add_f32_e32 v20, 1.0, v20
	v_rcp_f32_e32 v57, v20
	s_nop 0
	v_pk_mul_f32 v[54:55], v[56:57], v[54:55]
	s_nop 0
	v_pk_mul_f32 v[50:51], v[54:55], v[50:51]
	s_nop 0
	v_cvt_pk_bf16_f32 v20, v50, v51
	v_lshlrev_b32_e32 v50, 16, v21
	v_and_b32_e32 v51, 0xffff0000, v21
	v_mul_f32_e32 v21, 0xbfb8aa3b, v50
	v_exp_f32_e32 v21, v21
	s_nop 0
	v_add_f32_e32 v21, 1.0, v21
	v_rcp_f32_e32 v54, v21
	v_mul_f32_e32 v21, 0xbfb8aa3b, v51
	v_exp_f32_e32 v21, v21
	s_nop 0
	v_add_f32_e32 v21, 1.0, v21
	v_rcp_f32_e32 v55, v21
	s_nop 0
	v_pk_mul_f32 v[50:51], v[54:55], v[50:51]
	s_nop 0
	v_pk_mul_f32 v[50:51], v[50:51], v[52:53]
	s_nop 0
	v_cvt_pk_bf16_f32 v21, v50, v51
	v_lshlrev_b64 v[50:51], 11, v[68:69]
	v_lshl_add_u64 v[50:51], s[74:75], 0, v[50:51]
	v_lshl_add_u64 v[50:51], v[50:51], 0, v[58:59]
	global_store_dwordx4 v[50:51], v[18:21], off
	s_waitcnt vmcnt(1)
	s_nop 0
	v_mov_b64_e32 v[18:19], v[46:47]
	v_mov_b64_e32 v[20:21], v[48:49]
	s_cbranch_scc0 .LBB0_838
